# speedup vs baseline: 1.0132x; 1.0132x over previous
_Z7k2_elimPKjPKiPiS2_PfP15HIP_vector_typeIiLj4EEPKfS4_PtSA_:
	s_load_dwordx2 s[6:7], s[0:1], 0x8
	s_mov_b64 s[4:5], -1
	s_cmpk_lt_u32 s2, 0x80
	v_lshrrev_b32_e32 v1, 6, v0
	v_lshlrev_b32_e32 v14, 2, v0
	s_cbranch_scc0 .LBB1_28
	s_load_dwordx2 s[4:5], s[0:1], 0x0
	s_load_dwordx2 s[8:9], s[0:1], 0x18
	s_lshr_b32 s14, s2, 6
	s_mov_b32 s15, 0
	s_and_b32 s3, s2, 63
	s_lshl_b64 s[10:11], s[14:15], 11
	s_waitcnt lgkmcnt(0)
	s_add_u32 s8, s8, s10
	s_addc_u32 s9, s9, s11
	s_lshl_b32 s10, s3, 5
	s_add_u32 s8, s8, s10
	s_addc_u32 s9, s9, 0
	s_lshl_b64 s[10:11], s[14:15], 15
	s_add_u32 s4, s4, s10
	s_addc_u32 s5, s5, s11
	v_lshlrev_b32_e32 v2, 4, v0
	v_mov_b32_e32 v3, 0
	v_lshl_add_u64 v[4:5], s[4:5], 0, v[2:3]
	s_movk_i32 s10, 0x2000
	v_readfirstlane_b32 s46, v1
	s_mov_b64 s[44:45], 0x2000
	s_lshl_b32 s46, s46, 10
	s_mov_b32 m0, s46
	v_lshl_add_u64 v[20:21], v[4:5], 0, s[44:45]
	global_load_lds_dwordx4 v[4:5], off
	s_add_u32 s47, s46, 0x2000
	s_mov_b32 m0, s47
	v_lshl_add_u64 v[22:23], v[20:21], 0, s[44:45]
	global_load_lds_dwordx4 v[20:21], off
	s_add_u32 s47, s46, 0x4000
	s_mov_b32 m0, s47
	v_lshl_add_u64 v[20:21], v[22:23], 0, s[44:45]
	global_load_lds_dwordx4 v[22:23], off
	s_add_u32 s47, s46, 0x6000
	s_mov_b32 m0, s47
	s_movk_i32 s4, 0x1000
	global_load_lds_dwordx4 v[20:21], off
	v_lshl_or_b32 v4, s14, 12, v0
	v_mov_b32_e32 v5, v3
	v_lshl_add_u64 v[4:5], v[4:5], 2, s[6:7]
	v_add_co_u32_e32 v24, vcc, s4, v4
	s_cmp_lg_u32 s3, 0
	s_nop 0
	v_addc_co_u32_e32 v25, vcc, 0, v5, vcc
	v_add_co_u32_e32 v26, vcc, s10, v4
	s_nop 1
	v_addc_co_u32_e32 v27, vcc, 0, v5, vcc
	global_load_dword v15, v[26:27], off offset:-4096
	global_load_dword v28, v[26:27], off
	global_load_dword v29, v[26:27], off offset:2048
	v_add_co_u32_e32 v26, vcc, 0x3000, v4
	s_nop 1
	v_addc_co_u32_e32 v27, vcc, 0, v5, vcc
	global_load_dword v30, v[4:5], off
	global_load_dword v31, v[4:5], off offset:2048
	global_load_dword v32, v[24:25], off offset:2048
	global_load_dword v33, v[26:27], off
	global_load_dword v34, v[26:27], off offset:2048
	v_lshlrev_b32_e32 v4, 2, v1
	global_load_dword v5, v4, s[8:9]
	s_waitcnt vmcnt(4)
	v_max3_i32 v4, v30, v31, v15
	s_waitcnt vmcnt(3)
	v_max3_i32 v4, v4, v32, v28
	s_waitcnt vmcnt(2)
	v_max3_i32 v4, v4, v29, v33
	s_waitcnt vmcnt(1)
	v_max3_i32 v4, v4, v34, -1
	ds_write_b32 v14, v4 offset:32768
	s_cbranch_scc0 .LBB1_34
	v_or_b32_e32 v3, 0x8000, v14
	v_cmp_gt_u32_e32 vcc, 16, v0
	s_and_saveexec_b64 s[4:5], vcc

	.amdhsa_kernel _Z7k2_elimPKjPKiPiS2_PfP15HIP_vector_typeIiLj4EEPKfS4_PtSA_
		.amdhsa_group_segment_fixed_size 34880
		.amdhsa_private_segment_fixed_size 0
		.amdhsa_kernarg_size 80
		.amdhsa_user_sgpr_count 2
		.amdhsa_user_sgpr_dispatch_ptr 0
		.amdhsa_user_sgpr_queue_ptr 0
		.amdhsa_user_sgpr_kernarg_segment_ptr 1
		.amdhsa_user_sgpr_dispatch_id 0
		.amdhsa_user_sgpr_kernarg_preload_length 0
		.amdhsa_user_sgpr_kernarg_preload_offset 0
		.amdhsa_user_sgpr_private_segment_size 0
		.amdhsa_uses_dynamic_stack 0
		.amdhsa_enable_private_segment 0
		.amdhsa_system_sgpr_workgroup_id_x 1
		.amdhsa_system_sgpr_workgroup_id_y 0
		.amdhsa_system_sgpr_workgroup_id_z 0
		.amdhsa_system_sgpr_workgroup_info 0
		.amdhsa_system_vgpr_workitem_id 0
		.amdhsa_next_free_vgpr 35
		.amdhsa_next_free_sgpr 48
		.amdhsa_accum_offset 36
		.amdhsa_reserve_vcc 1
		.amdhsa_float_round_mode_32 0
		.amdhsa_float_round_mode_16_64 0
		.amdhsa_float_denorm_mode_32 3
		.amdhsa_float_denorm_mode_16_64 3
		.amdhsa_dx10_clamp 1
		.amdhsa_ieee_mode 1
		.amdhsa_fp16_overflow 0
		.amdhsa_tg_split 0
		.amdhsa_exception_fp_ieee_invalid_op 0
		.amdhsa_exception_fp_denorm_src 0
		.amdhsa_exception_fp_ieee_div_zero 0
		.amdhsa_exception_fp_ieee_overflow 0
		.amdhsa_exception_fp_ieee_underflow 0
		.amdhsa_exception_fp_ieee_inexact 0
		.amdhsa_exception_int_div_zero 0
	.end_amdhsa_kernel

amdhsa.kernels:
  - .agpr_count:     0
    .args:
      - .actual_access:  read_only
        .address_space:  global
        .offset:         0
        .size:           8
        .value_kind:     global_buffer
      - .actual_access:  read_only
        .address_space:  global
        .offset:         8
        .size:           8
        .value_kind:     global_buffer
      - .actual_access:  write_only
        .address_space:  global
        .offset:         16
        .size:           8
        .value_kind:     global_buffer
      - .actual_access:  write_only
        .address_space:  global
        .offset:         24
        .size:           8
        .value_kind:     global_buffer
      - .actual_access:  write_only
        .address_space:  global
        .offset:         32
        .size:           8
        .value_kind:     global_buffer
    .group_segment_fixed_size: 1024
    .kernarg_segment_align: 8
    .kernarg_segment_size: 40
    .language:       OpenCL C
    .language_version:
      - 2
      - 0
    .max_flat_workgroup_size: 256
    .name:           _Z7k1_packPKfS0_PmPiP15HIP_vector_typeIfLj4EE
    .private_segment_fixed_size: 0
    .sgpr_count:     16
    .sgpr_spill_count: 0
    .symbol:         _Z7k1_packPKfS0_PmPiP15HIP_vector_typeIfLj4EE.kd
    .uniform_work_group_size: 1
    .uses_dynamic_stack: false
    .vgpr_count:     33
    .vgpr_spill_count: 0
    .wavefront_size: 64
  - .agpr_count:     0
    .args:
      - .actual_access:  read_only
        .address_space:  global
        .offset:         0
        .size:           8
        .value_kind:     global_buffer
      - .actual_access:  read_only
        .address_space:  global
        .offset:         8
        .size:           8
        .value_kind:     global_buffer
      - .actual_access:  write_only
        .address_space:  global
        .offset:         16
        .size:           8
        .value_kind:     global_buffer
      - .actual_access:  read_only
        .address_space:  global
        .offset:         24
        .size:           8
        .value_kind:     global_buffer
      - .actual_access:  write_only
        .address_space:  global
        .offset:         32
        .size:           8
        .value_kind:     global_buffer
      - .actual_access:  write_only
        .address_space:  global
        .offset:         40
        .size:           8
        .value_kind:     global_buffer
      - .actual_access:  read_only
        .address_space:  global
        .offset:         48
        .size:           8
        .value_kind:     global_buffer
      - .address_space:  global
        .offset:         56
        .size:           8
        .value_kind:     global_buffer
      - .actual_access:  write_only
        .address_space:  global
        .offset:         64
        .size:           8
        .value_kind:     global_buffer
      - .actual_access:  write_only
        .address_space:  global
        .offset:         72
        .size:           8
        .value_kind:     global_buffer
    .group_segment_fixed_size: 34880
    .kernarg_segment_align: 8
    .kernarg_segment_size: 80
    .language:       OpenCL C
    .language_version:
      - 2
      - 0
    .max_flat_workgroup_size: 512
    .name:           _Z7k2_elimPKjPKiPiS2_PfP15HIP_vector_typeIiLj4EEPKfS4_PtSA_
    .private_segment_fixed_size: 0
    .sgpr_count:     54
    .sgpr_spill_count: 0
    .symbol:         _Z7k2_elimPKjPKiPiS2_PfP15HIP_vector_typeIiLj4EEPKfS4_PtSA_.kd
    .uniform_work_group_size: 1
    .uses_dynamic_stack: false
    .vgpr_count:     35
    .vgpr_spill_count: 0
    .wavefront_size: 64
  - .agpr_count:     0
    .args:
      - .actual_access:  read_only
        .address_space:  global
        .offset:         0
        .size:           8
        .value_kind:     global_buffer
      - .actual_access:  read_only
        .address_space:  global
        .offset:         8
        .size:           8
        .value_kind:     global_buffer
      - .actual_access:  read_only
        .address_space:  global
        .offset:         16
        .size:           8
        .value_kind:     global_buffer
      - .actual_access:  read_only
        .address_space:  global
        .offset:         24
        .size:           8
        .value_kind:     global_buffer
      - .actual_access:  read_only
        .address_space:  global
        .offset:         32
        .size:           8
        .value_kind:     global_buffer
      - .actual_access:  read_only
        .address_space:  global
        .offset:         40
        .size:           8
        .value_kind:     global_buffer
      - .actual_access:  write_only
        .address_space:  global
        .offset:         48
        .size:           8
        .value_kind:     global_buffer
    .group_segment_fixed_size: 80064
    .kernarg_segment_align: 8
    .kernarg_segment_size: 56
    .language:       OpenCL C
    .language_version:
      - 2
      - 0
    .max_flat_workgroup_size: 256
    .name:           _Z8k3_chainPKfPK15HIP_vector_typeIiLj4EEPKtS6_S0_S0_Pf
    .private_segment_fixed_size: 0
    .sgpr_count:     28
    .sgpr_spill_count: 0
    .symbol:         _Z8k3_chainPKfPK15HIP_vector_typeIiLj4EEPKtS6_S0_S0_Pf.kd
    .uniform_work_group_size: 1
    .uses_dynamic_stack: false
    .vgpr_count:     184
    .vgpr_spill_count: 0
    .wavefront_size: 64
